# grid barrier between PREP1 and UP2 removed (independent phases: both only read P, write disjoint buffers); loops as previous version
# speedup vs baseline: 1.0137x; 1.0024x over previous
.LBB0_778:
	s_mul_i32 s0, s24, 11
	s_add_i32 s0, s0, 4
	s_cmp_ge_i32 s0, s93
	s_branch .LBB0_832
	v_mbcnt_lo_u32_b32 v0, -1, 0
	v_mbcnt_hi_u32_b32 v0, -1, v0
	s_waitcnt vmcnt(0)
	v_readlane_b32 s0, v251, 4
	v_sub_u32_e32 v0, 0, v0
	s_waitcnt vmcnt(0)
	v_cmp_eq_u32_e32 vcc, s0, v0
	s_barrier
	s_and_saveexec_b64 s[0:1], vcc
	s_cbranch_execz .LBB0_831
	v_readlane_b32 s2, v253, 5
	s_waitcnt vmcnt(0) expcnt(0) lgkmcnt(0)
	s_nop 0
	v_mov_b32_e32 v0, s2
	ds_read_b32 v3, v0
	v_readlane_b32 s2, v253, 6
	s_waitcnt lgkmcnt(0)
	v_cmp_ne_u32_e32 vcc, 0, v3
	v_mov_b32_e32 v0, s2
	ds_read_b32 v2, v0
	s_cbranch_vccnz .LBB0_795
	v_readlane_b32 s4, v251, 0
	v_readlane_b32 s5, v251, 1
	s_load_dwordx2 s[2:3], s[4:5], 0x4
	s_mov_b32 s9, 1
	s_waitcnt lgkmcnt(0)
	s_mul_i32 s8, s2, s70
	s_mul_i32 s8, s8, s3
	s_branch .LBB0_783
